# speedup vs baseline: 1.0033x; 1.0033x over previous
_Z17conv_xproj_kernelPKDF16_PKfS2_S0_PDF16_S3_Pf:
	s_load_dwordx8 s[4:11], s[0:1], 0x0
	s_load_dwordx2 s[14:15], s[0:1], 0x20
	s_load_dwordx4 s[20:23], s[0:1], 0x28
	s_lshl_b32 s12, s2, 4
	s_and_b32 s3, s2, 0x7f
	v_lshlrev_b32_e32 v60, 4, v0
	v_lshrrev_b32_e32 v61, 6, v0
	v_and_b32_e32 v59, 63, v0
	v_mul_u32_u24_e32 v58, 0x600, v61
	v_or_b32_e32 v59, v58, v59
	v_lshlrev_b32_e32 v59, 4, v59
	s_waitcnt lgkmcnt(0)
	s_lshl_b32 s13, s2, 17
	s_add_u32 s16, s4, s13
	s_addc_u32 s17, s5, 0
	s_cmp_eq_u32 s3, 0
	s_cbranch_scc1 .Lcx_first
	s_sub_u32 s18, s16, 0x8000
	s_subb_u32 s19, s17, 0
	global_load_dwordx4 v[2:5], v60, s[18:19]
	s_branch .Lcx_go

.LBB1_5:
	s_or_b64 exec, exec, s[2:3]
	s_mov_b64 s[2:3], s[20:21]
	s_movk_i32 s4, 0x200
	v_cmp_gt_u32_e32 vcc, s4, v0
	s_waitcnt lgkmcnt(0)
	s_barrier
	s_and_saveexec_b64 s[4:5], vcc
	s_cbranch_execz .LBB1_7
	s_movk_i32 s6, 0x184
	v_mad_u32_u24 v1, v1, s6, v30
	ds_read2_b32 v[26:27], v1 offset1:1
	ds_read2_b32 v[28:29], v1 offset0:2 offset1:3
	ds_read2_b32 v[30:31], v1 offset0:16 offset1:17
	ds_read2_b32 v[32:33], v1 offset0:18 offset1:19
	s_waitcnt lgkmcnt(3)
	v_pk_add_f32 v[22:23], v[22:23], v[26:27]
	s_waitcnt lgkmcnt(2)
	v_pk_add_f32 v[24:25], v[24:25], v[28:29]
	s_waitcnt lgkmcnt(1)
	v_pk_add_f32 v[18:19], v[18:19], v[30:31]
	ds_write2_b32 v1, v22, v23 offset1:1
	ds_write2_b32 v1, v24, v25 offset0:2 offset1:3
	ds_write2_b32 v1, v18, v19 offset0:16 offset1:17
	s_waitcnt lgkmcnt(3)
	v_pk_add_f32 v[18:19], v[20:21], v[32:33]
	ds_read2_b32 v[20:21], v1 offset0:32 offset1:33
	ds_write2_b32 v1, v18, v19 offset0:18 offset1:19
	ds_read2_b32 v[18:19], v1 offset0:34 offset1:35
	ds_read2_b32 v[22:23], v1 offset0:48 offset1:49
	ds_read2_b32 v[24:25], v1 offset0:50 offset1:51
	s_waitcnt lgkmcnt(4)
	v_pk_add_f32 v[14:15], v[14:15], v[20:21]
	s_waitcnt lgkmcnt(1)
	v_pk_add_f32 v[10:11], v[10:11], v[22:23]
	ds_write2_b32 v1, v14, v15 offset0:32 offset1:33
	v_pk_add_f32 v[14:15], v[16:17], v[18:19]
	ds_write2_b32 v1, v10, v11 offset0:48 offset1:49
	s_waitcnt lgkmcnt(2)
	v_pk_add_f32 v[10:11], v[12:13], v[24:25]
	ds_write2_b32 v1, v14, v15 offset0:34 offset1:35
	ds_read2_b32 v[12:13], v1 offset0:64 offset1:65
	ds_write2_b32 v1, v10, v11 offset0:50 offset1:51
	ds_read2_b32 v[10:11], v1 offset0:66 offset1:67
	ds_read2_b32 v[14:15], v1 offset0:80 offset1:81
	ds_read2_b32 v[16:17], v1 offset0:82 offset1:83
	s_waitcnt lgkmcnt(4)
	v_pk_add_f32 v[6:7], v[6:7], v[12:13]
	s_waitcnt lgkmcnt(1)
	v_pk_add_f32 v[2:3], v[2:3], v[14:15]
	ds_write2_b32 v1, v6, v7 offset0:64 offset1:65
	v_pk_add_f32 v[6:7], v[8:9], v[10:11]
	ds_write2_b32 v1, v2, v3 offset0:80 offset1:81
	s_waitcnt lgkmcnt(2)
	v_pk_add_f32 v[2:3], v[4:5], v[16:17]
	ds_write2_b32 v1, v6, v7 offset0:66 offset1:67
	ds_write2_b32 v1, v2, v3 offset0:82 offset1:83
.LBB1_7:
	s_or_b64 exec, exec, s[4:5]
	s_mov_b64 s[0:1], s[22:23]
	s_ashr_i32 s13, s12, 31
	s_mov_b64 s[4:5], 0
	s_mov_b32 s8, 0xaaab
	v_mov_b32_e32 v3, 0
	s_movk_i32 s9, 0x1ff
	s_waitcnt lgkmcnt(0)
	s_barrier
	s_branch .LBB1_9

	.amdhsa_kernel _Z17conv_xproj_kernelPKDF16_PKfS2_S0_PDF16_S3_Pf
		.amdhsa_group_segment_fixed_size 65792
		.amdhsa_private_segment_fixed_size 0
		.amdhsa_kernarg_size 56
		.amdhsa_user_sgpr_count 2
		.amdhsa_user_sgpr_dispatch_ptr 0
		.amdhsa_user_sgpr_queue_ptr 0
		.amdhsa_user_sgpr_kernarg_segment_ptr 1
		.amdhsa_user_sgpr_dispatch_id 0
		.amdhsa_user_sgpr_kernarg_preload_length 0
		.amdhsa_user_sgpr_kernarg_preload_offset 0
		.amdhsa_user_sgpr_private_segment_size 0
		.amdhsa_uses_dynamic_stack 0
		.amdhsa_enable_private_segment 0
		.amdhsa_system_sgpr_workgroup_id_x 1
		.amdhsa_system_sgpr_workgroup_id_y 0
		.amdhsa_system_sgpr_workgroup_id_z 0
		.amdhsa_system_sgpr_workgroup_info 0
		.amdhsa_system_vgpr_workitem_id 0
		.amdhsa_next_free_vgpr 128
		.amdhsa_next_free_sgpr 24
		.amdhsa_accum_offset 128
		.amdhsa_reserve_vcc 1
		.amdhsa_float_round_mode_32 0
		.amdhsa_float_round_mode_16_64 0
		.amdhsa_float_denorm_mode_32 3
		.amdhsa_float_denorm_mode_16_64 3
		.amdhsa_dx10_clamp 1
		.amdhsa_ieee_mode 1
		.amdhsa_fp16_overflow 0
		.amdhsa_tg_split 0
		.amdhsa_exception_fp_ieee_invalid_op 0
		.amdhsa_exception_fp_denorm_src 0
		.amdhsa_exception_fp_ieee_div_zero 0
		.amdhsa_exception_fp_ieee_overflow 0
		.amdhsa_exception_fp_ieee_underflow 0
		.amdhsa_exception_fp_ieee_inexact 0
		.amdhsa_exception_int_div_zero 0
	.end_amdhsa_kernel

_Z11gemm_8phaseILi0ELi16ELi16ELi1024ELi1024ELi4096ELi1EEvPKDF16_S1_PvS2_fPj:
	s_load_dwordx4 s[4:7], s[0:1], 0x0
	s_load_dword s32, s[0:1], 0x20
	s_and_b32 s3, s2, 7
	s_lshl_b32 s3, s3, 5
	s_lshr_b32 s8, s2, 3
	s_add_i32 s2, s3, s8
	s_and_b32 s3, s2, 127
	s_lshr_b32 s8, s2, 7
	s_lshl_b32 s8, s8, 3
	s_and_b32 s9, s3, 7
	s_add_i32 s10, s8, s9
	s_lshr_b32 s3, s3, 3
	s_mov_b32 s9, s3
	s_mov_b32 s8, 0
	v_lshrrev_b32_e32 v2, 3, v0
	v_and_b32_e32 v4, 48, v2
	v_bfe_u32 v5, v0, 2, 4
	s_lshl_b32 s28, s10, 8
	v_or_b32_e32 v9, v4, v5
	v_or_b32_e32 v2, s28, v9
	s_lshl_b32 s29, s3, 7
	v_ashrrev_i32_e32 v3, 31, v2
	v_lshlrev_b64 v[10:11], 11, v[2:3]
	v_or_b32_e32 v2, s29, v9
	v_lshlrev_b32_e32 v6, 4, v0
	v_and_b32_e32 v1, 32, v0
	v_ashrrev_i32_e32 v3, 31, v2
	s_add_i32 s10, 0, 0x10000
	v_bitop3_b32 v7, v6, v1, 48 bitop3:0x6c
	v_and_b32_e32 v8, 64, v0
	v_lshlrev_b64 v[2:3], 11, v[2:3]
	v_add_u32_e32 v145, s10, v6
	v_or_b32_e32 v130, v7, v8
	v_mov_b32_e32 v131, 0
	s_waitcnt lgkmcnt(0)
	v_lshl_add_u64 v[2:3], s[6:7], 0, v[2:3]
	v_readfirstlane_b32 s2, v145
	v_add_u32_e32 v146, 0x2000, v145
	v_lshl_add_u64 v[2:3], v[2:3], 0, v[130:131]
	s_mov_b32 m0, s2
	s_mov_b64 s[2:3], 0x20000
	v_readfirstlane_b32 s11, v146
	v_lshl_add_u64 v[10:11], s[4:5], 0, v[10:11]
	v_add_u32_e32 v144, 0, v6
	global_load_lds_dwordx4 v[2:3], off
	v_lshl_add_u64 v[12:13], v[2:3], 0, s[2:3]
	s_mov_b32 m0, s11
	v_lshl_add_u64 v[132:133], v[10:11], 0, v[130:131]
	v_readfirstlane_b32 s11, v144
	v_add_u32_e32 v147, 0x2000, v144
	global_load_lds_dwordx4 v[12:13], off
	s_mov_b32 m0, s11
	v_lshl_add_u64 v[10:11], v[132:133], 0, s[2:3]
	v_readfirstlane_b32 s2, v147
	s_add_i32 s11, 0, 0x14000
	global_load_lds_dwordx4 v[132:133], off
	s_mov_b32 m0, s2
	v_add_u32_e32 v149, s11, v6
	s_mov_b64 s[2:3], 0x400000
	global_load_lds_dwordx4 v[10:11], off
	v_lshl_add_u64 v[10:11], v[2:3], 0, s[2:3]
	v_readfirstlane_b32 s2, v149
	s_mov_b32 m0, s2
	s_mov_b64 s[2:3], 0x420000
	v_add_u32_e32 v150, 0x2000, v149
	global_load_lds_dwordx4 v[10:11], off
	v_lshl_add_u64 v[10:11], v[2:3], 0, s[2:3]
	v_readfirstlane_b32 s2, v150
	s_mov_b32 m0, s2
	v_add_u32_e32 v151, 0x4000, v144
	s_mov_b64 s[2:3], 0x40000
	global_load_lds_dwordx4 v[10:11], off
	v_lshl_add_u64 v[10:11], v[132:133], 0, s[2:3]
	v_readfirstlane_b32 s2, v151
	s_mov_b32 m0, s2
	s_mov_b64 s[2:3], 0x60000
	v_add_u32_e32 v153, 0x6000, v144
	global_load_lds_dwordx4 v[10:11], off
	v_lshl_add_u64 v[10:11], v[132:133], 0, s[2:3]
	v_readfirstlane_b32 s2, v153
	s_mov_b32 m0, s2
	v_lshrrev_b32_e32 v9, 8, v0
	global_load_lds_dwordx4 v[10:11], off
	v_cmp_eq_u32_e32 vcc, 1, v9
	s_and_saveexec_b64 s[2:3], vcc
	s_cbranch_execz .LBB5_6
	s_barrier

.LBB5_10:
	s_or_b64 exec, exec, s[4:5]
	s_mov_b32 s0, s32
	v_and_b32_e32 v0, 12, v154
	v_or3_b32 v132, v0, v138, s28
	v_ashrrev_i32_e32 v130, 2, v132
	v_lshlrev_b32_e32 v0, 5, v1
	v_ashrrev_i32_e32 v131, 31, v130
	v_or3_b32 v134, s29, v0, v152
	v_lshlrev_b64 v[0:1], 15, v[130:131]
	v_lshl_add_u64 v[136:137], s[2:3], 0, v[0:1]
	s_waitcnt lgkmcnt(0)
	v_pk_mul_f32 v[0:1], s[0:1], v[128:129] op_sel_hi:[0,1]
	v_ashrrev_i32_e32 v135, 31, v134
	v_pk_mul_f32 v[126:127], s[0:1], v[126:127] op_sel_hi:[0,1]
	v_cvt_pk_f16_f32 v129, v0, v1
	v_lshlrev_b64 v[0:1], 3, v[134:135]
	v_cvt_pk_f16_f32 v128, v126, v127
	v_lshl_add_u64 v[126:127], v[136:137], 0, v[0:1]
	global_store_dwordx2 v[126:127], v[128:129], off
	v_or_b32_e32 v126, 16, v134
	v_pk_mul_f32 v[120:121], s[0:1], v[120:121] op_sel_hi:[0,1]
	v_pk_mul_f32 v[118:119], s[0:1], v[118:119] op_sel_hi:[0,1]
	v_ashrrev_i32_e32 v127, 31, v126
	v_cvt_pk_f16_f32 v121, v120, v121
	v_cvt_pk_f16_f32 v120, v118, v119
	v_lshlrev_b64 v[118:119], 3, v[126:127]
	v_lshl_add_u64 v[126:127], v[136:137], 0, v[118:119]
	v_pk_mul_f32 v[122:123], s[0:1], v[122:123] op_sel_hi:[0,1]
	global_store_dwordx2 v[126:127], v[120:121], off
	v_mul_f32_e32 v121, 0xbfb8aa3b, v122
	v_pk_mul_f32 v[124:125], s[0:1], v[124:125] op_sel_hi:[0,1]
	v_exp_f32_e32 v121, v121
	v_mul_f32_e32 v126, 0xbfb8aa3b, v123
	v_mul_f32_e32 v127, 0xbfb8aa3b, v124
	v_exp_f32_e32 v126, v126
	v_exp_f32_e32 v127, v127
	v_mul_f32_e32 v128, 0xbfb8aa3b, v125
	v_exp_f32_e32 v128, v128
	v_add_f32_e32 v121, 1.0, v121
	v_rcp_f32_e32 v121, v121
	v_add_f32_e32 v126, 1.0, v126
	v_add_f32_e32 v127, 1.0, v127
	v_rcp_f32_e32 v126, v126
	v_rcp_f32_e32 v127, v127
	v_add_f32_e32 v128, 1.0, v128
	v_rcp_f32_e32 v128, v128
	v_fma_mixlo_f16 v121, v122, v121, 0
	v_pk_mov_b32 v[122:123], v[122:123], v[124:125] op_sel:[1,0]
	v_add_u32_e32 v120, 0x800, v134
	v_pk_mul_f32 v[122:123], v[122:123], v[126:127]
	v_pk_mul_f32 v[114:115], s[0:1], v[114:115] op_sel_hi:[0,1]
	v_cvt_pk_f16_f32 v123, v122, v123
	v_pack_b32_f16 v122, v121, v123
	v_fma_mixlo_f16 v121, v125, v128, 0
	v_alignbit_b32 v123, v121, v123, 16
	v_ashrrev_i32_e32 v121, 31, v120
	v_lshlrev_b64 v[120:121], 3, v[120:121]
	v_lshl_add_u64 v[124:125], v[136:137], 0, v[120:121]
	global_store_dwordx2 v[124:125], v[122:123], off
	v_mul_f32_e32 v123, 0xbfb8aa3b, v114
	v_pk_mul_f32 v[116:117], s[0:1], v[116:117] op_sel_hi:[0,1]
	v_exp_f32_e32 v123, v123
	v_mul_f32_e32 v124, 0xbfb8aa3b, v115
	v_mul_f32_e32 v125, 0xbfb8aa3b, v116
	v_exp_f32_e32 v124, v124
	v_exp_f32_e32 v125, v125
	v_mul_f32_e32 v126, 0xbfb8aa3b, v117
	v_exp_f32_e32 v126, v126
	v_add_f32_e32 v123, 1.0, v123
	v_rcp_f32_e32 v123, v123
	v_add_f32_e32 v124, 1.0, v124
	v_add_f32_e32 v125, 1.0, v125
	v_rcp_f32_e32 v124, v124
	v_rcp_f32_e32 v125, v125
	v_add_f32_e32 v126, 1.0, v126
	v_rcp_f32_e32 v126, v126
	v_fma_mixlo_f16 v123, v114, v123, 0
	v_pk_mov_b32 v[114:115], v[114:115], v[116:117] op_sel:[1,0]
	v_add_u32_e32 v122, 0x810, v134
	v_pk_mul_f32 v[114:115], v[114:115], v[124:125]
	v_pk_mul_f32 v[104:105], s[0:1], v[104:105] op_sel_hi:[0,1]
	v_cvt_pk_f16_f32 v114, v114, v115
	v_pack_b32_f16 v116, v123, v114
	v_fma_mixlo_f16 v115, v117, v126, 0
	v_ashrrev_i32_e32 v123, 31, v122
	v_alignbit_b32 v117, v115, v114, 16
	v_lshlrev_b64 v[114:115], 3, v[122:123]
	v_lshl_add_u64 v[122:123], v[136:137], 0, v[114:115]
	global_store_dwordx2 v[122:123], v[116:117], off
	v_or_b32_e32 v116, 4, v130
	v_ashrrev_i32_e32 v117, 31, v116
	v_lshlrev_b64 v[116:117], 15, v[116:117]
	v_lshl_add_u64 v[116:117], s[2:3], 0, v[116:117]
	v_pk_mul_f32 v[102:103], s[0:1], v[102:103] op_sel_hi:[0,1]
	v_cvt_pk_f16_f32 v105, v104, v105
	v_cvt_pk_f16_f32 v104, v102, v103
	v_lshl_add_u64 v[102:103], v[116:117], 0, v[118:119]
	global_store_dwordx2 v[102:103], v[104:105], off
	v_pk_mul_f32 v[102:103], s[0:1], v[106:107] op_sel_hi:[0,1]
	v_mul_f32_e32 v104, 0xbfb8aa3b, v102
	v_exp_f32_e32 v106, v104
	v_mul_f32_e32 v104, 0xbfb8aa3b, v103
	v_exp_f32_e32 v107, v104
	v_pk_mul_f32 v[104:105], s[0:1], v[108:109] op_sel_hi:[0,1]
	v_add_f32_e32 v106, 1.0, v106
	v_rcp_f32_e32 v108, v106
	v_add_f32_e32 v106, 1.0, v107
	v_mul_f32_e32 v107, 0xbfb8aa3b, v104
	v_exp_f32_e32 v107, v107
	v_mul_f32_e32 v109, 0xbfb8aa3b, v105
	v_exp_f32_e32 v109, v109
	v_rcp_f32_e32 v106, v106
	v_add_f32_e32 v107, 1.0, v107
	v_rcp_f32_e32 v107, v107
	v_add_f32_e32 v109, 1.0, v109
	v_rcp_f32_e32 v109, v109
	v_fma_mixlo_f16 v108, v102, v108, 0
	v_pk_mov_b32 v[102:103], v[102:103], v[104:105] op_sel:[1,0]
	v_pk_mul_f32 v[98:99], s[0:1], v[98:99] op_sel_hi:[0,1]
	v_pk_mul_f32 v[102:103], v[102:103], v[106:107]
	v_fma_mixlo_f16 v104, v105, v109, 0
	v_cvt_pk_f16_f32 v103, v102, v103
	v_pack_b32_f16 v102, v108, v103
	v_alignbit_b32 v103, v104, v103, 16
	v_lshl_add_u64 v[104:105], v[116:117], 0, v[120:121]
	global_store_dwordx2 v[104:105], v[102:103], off
	v_mul_f32_e32 v102, 0xbfb8aa3b, v98
	v_exp_f32_e32 v102, v102
	v_mul_f32_e32 v103, 0xbfb8aa3b, v99
	v_exp_f32_e32 v103, v103
	v_pk_mul_f32 v[100:101], s[0:1], v[100:101] op_sel_hi:[0,1]
	v_add_f32_e32 v102, 1.0, v102
	v_rcp_f32_e32 v104, v102
	v_add_f32_e32 v102, 1.0, v103
	v_mul_f32_e32 v103, 0xbfb8aa3b, v100
	v_exp_f32_e32 v103, v103
	v_mul_f32_e32 v105, 0xbfb8aa3b, v101
	v_exp_f32_e32 v105, v105
	v_rcp_f32_e32 v102, v102
	v_add_f32_e32 v103, 1.0, v103
	v_rcp_f32_e32 v103, v103
	v_add_f32_e32 v105, 1.0, v105
	v_rcp_f32_e32 v105, v105
	v_fma_mixlo_f16 v104, v98, v104, 0
	v_pk_mov_b32 v[98:99], v[98:99], v[100:101] op_sel:[1,0]
	v_pk_mul_f32 v[88:89], s[0:1], v[88:89] op_sel_hi:[0,1]
	v_pk_mul_f32 v[98:99], v[98:99], v[102:103]
	v_fma_mixlo_f16 v100, v101, v105, 0
	v_cvt_pk_f16_f32 v99, v98, v99
	v_pack_b32_f16 v98, v104, v99
	v_alignbit_b32 v99, v100, v99, 16
	v_lshl_add_u64 v[100:101], v[116:117], 0, v[114:115]
	global_store_dwordx2 v[100:101], v[98:99], off
	v_or_b32_e32 v98, 8, v130
	v_ashrrev_i32_e32 v99, 31, v98
	v_lshlrev_b64 v[98:99], 15, v[98:99]
	v_lshl_add_u64 v[98:99], s[2:3], 0, v[98:99]
	v_pk_mul_f32 v[86:87], s[0:1], v[86:87] op_sel_hi:[0,1]
	v_cvt_pk_f16_f32 v89, v88, v89
	v_cvt_pk_f16_f32 v88, v86, v87
	v_lshl_add_u64 v[86:87], v[98:99], 0, v[118:119]
	global_store_dwordx2 v[86:87], v[88:89], off
	v_pk_mul_f32 v[86:87], s[0:1], v[90:91] op_sel_hi:[0,1]
	v_mul_f32_e32 v88, 0xbfb8aa3b, v86
	v_exp_f32_e32 v90, v88
	v_mul_f32_e32 v88, 0xbfb8aa3b, v87
	v_exp_f32_e32 v91, v88
	v_pk_mul_f32 v[88:89], s[0:1], v[92:93] op_sel_hi:[0,1]
	v_add_f32_e32 v90, 1.0, v90
	v_rcp_f32_e32 v92, v90
	v_add_f32_e32 v90, 1.0, v91
	v_mul_f32_e32 v91, 0xbfb8aa3b, v88
	v_exp_f32_e32 v91, v91
	v_mul_f32_e32 v93, 0xbfb8aa3b, v89
	v_exp_f32_e32 v93, v93
	v_rcp_f32_e32 v90, v90
	v_add_f32_e32 v91, 1.0, v91
	v_rcp_f32_e32 v91, v91
	v_add_f32_e32 v93, 1.0, v93
	v_rcp_f32_e32 v93, v93
	v_fma_mixlo_f16 v92, v86, v92, 0
	v_pk_mov_b32 v[86:87], v[86:87], v[88:89] op_sel:[1,0]
	v_pk_mul_f32 v[112:113], s[0:1], v[112:113] op_sel_hi:[0,1]
	v_pk_mul_f32 v[86:87], v[86:87], v[90:91]
	v_pk_mul_f32 v[110:111], s[0:1], v[110:111] op_sel_hi:[0,1]
	v_cvt_pk_f16_f32 v87, v86, v87
	v_fma_mixlo_f16 v88, v89, v93, 0
	v_cvt_pk_f16_f32 v113, v112, v113
	v_cvt_pk_f16_f32 v112, v110, v111
	v_lshl_add_u64 v[110:111], v[116:117], 0, v[0:1]
	v_pack_b32_f16 v86, v92, v87
	v_alignbit_b32 v87, v88, v87, 16
	v_lshl_add_u64 v[88:89], v[98:99], 0, v[120:121]
	v_pk_mul_f32 v[82:83], s[0:1], v[82:83] op_sel_hi:[0,1]
	global_store_dwordx2 v[110:111], v[112:113], off
	global_store_dwordx2 v[88:89], v[86:87], off
	v_mul_f32_e32 v86, 0xbfb8aa3b, v82
	v_exp_f32_e32 v86, v86
	v_mul_f32_e32 v87, 0xbfb8aa3b, v83
	v_exp_f32_e32 v87, v87
	v_pk_mul_f32 v[84:85], s[0:1], v[84:85] op_sel_hi:[0,1]
	v_add_f32_e32 v86, 1.0, v86
	v_rcp_f32_e32 v88, v86
	v_add_f32_e32 v86, 1.0, v87
	v_mul_f32_e32 v87, 0xbfb8aa3b, v84
	v_exp_f32_e32 v87, v87
	v_mul_f32_e32 v89, 0xbfb8aa3b, v85
	v_exp_f32_e32 v89, v89
	v_rcp_f32_e32 v86, v86
	v_add_f32_e32 v87, 1.0, v87
	v_rcp_f32_e32 v87, v87
	v_add_f32_e32 v89, 1.0, v89
	v_rcp_f32_e32 v89, v89
	v_fma_mixlo_f16 v88, v82, v88, 0
	v_pk_mov_b32 v[82:83], v[82:83], v[84:85] op_sel:[1,0]
	v_pk_mul_f32 v[72:73], s[0:1], v[72:73] op_sel_hi:[0,1]
	v_pk_mul_f32 v[82:83], v[82:83], v[86:87]
	v_fma_mixlo_f16 v84, v85, v89, 0
	v_cvt_pk_f16_f32 v83, v82, v83
	v_pack_b32_f16 v82, v88, v83
	v_alignbit_b32 v83, v84, v83, 16
	v_lshl_add_u64 v[84:85], v[98:99], 0, v[114:115]
	global_store_dwordx2 v[84:85], v[82:83], off
	v_or_b32_e32 v82, 12, v130
	v_ashrrev_i32_e32 v83, 31, v82
	v_lshlrev_b64 v[82:83], 15, v[82:83]
	v_lshl_add_u64 v[82:83], s[2:3], 0, v[82:83]
	v_pk_mul_f32 v[70:71], s[0:1], v[70:71] op_sel_hi:[0,1]
	v_cvt_pk_f16_f32 v73, v72, v73
	v_cvt_pk_f16_f32 v72, v70, v71
	v_lshl_add_u64 v[70:71], v[82:83], 0, v[118:119]
	global_store_dwordx2 v[70:71], v[72:73], off
	v_pk_mul_f32 v[70:71], s[0:1], v[74:75] op_sel_hi:[0,1]
	v_mul_f32_e32 v72, 0xbfb8aa3b, v70
	v_exp_f32_e32 v74, v72
	v_mul_f32_e32 v72, 0xbfb8aa3b, v71
	v_exp_f32_e32 v75, v72
	v_pk_mul_f32 v[72:73], s[0:1], v[76:77] op_sel_hi:[0,1]
	v_add_f32_e32 v74, 1.0, v74
	v_rcp_f32_e32 v76, v74
	v_add_f32_e32 v74, 1.0, v75
	v_mul_f32_e32 v75, 0xbfb8aa3b, v72
	v_exp_f32_e32 v75, v75
	v_mul_f32_e32 v77, 0xbfb8aa3b, v73
	v_exp_f32_e32 v77, v77
	v_rcp_f32_e32 v74, v74
	v_add_f32_e32 v75, 1.0, v75
	v_rcp_f32_e32 v75, v75
	v_add_f32_e32 v77, 1.0, v77
	v_rcp_f32_e32 v77, v77
	v_fma_mixlo_f16 v76, v70, v76, 0
	v_pk_mov_b32 v[70:71], v[70:71], v[72:73] op_sel:[1,0]
	v_pk_mul_f32 v[96:97], s[0:1], v[96:97] op_sel_hi:[0,1]
	v_pk_mul_f32 v[70:71], v[70:71], v[74:75]
	v_pk_mul_f32 v[94:95], s[0:1], v[94:95] op_sel_hi:[0,1]
	v_cvt_pk_f16_f32 v71, v70, v71
	v_fma_mixlo_f16 v72, v73, v77, 0
	v_cvt_pk_f16_f32 v97, v96, v97
	v_cvt_pk_f16_f32 v96, v94, v95
	v_lshl_add_u64 v[94:95], v[98:99], 0, v[0:1]
	v_pack_b32_f16 v70, v76, v71
	v_alignbit_b32 v71, v72, v71, 16
	v_lshl_add_u64 v[72:73], v[82:83], 0, v[120:121]
	v_pk_mul_f32 v[66:67], s[0:1], v[66:67] op_sel_hi:[0,1]
	global_store_dwordx2 v[94:95], v[96:97], off
	global_store_dwordx2 v[72:73], v[70:71], off
	v_mul_f32_e32 v70, 0xbfb8aa3b, v66
	v_exp_f32_e32 v70, v70
	v_mul_f32_e32 v71, 0xbfb8aa3b, v67
	v_exp_f32_e32 v71, v71
	v_pk_mul_f32 v[68:69], s[0:1], v[68:69] op_sel_hi:[0,1]
	v_add_f32_e32 v70, 1.0, v70
	v_rcp_f32_e32 v72, v70
	v_add_f32_e32 v70, 1.0, v71
	v_mul_f32_e32 v71, 0xbfb8aa3b, v68
	v_exp_f32_e32 v71, v71
	v_mul_f32_e32 v73, 0xbfb8aa3b, v69
	v_exp_f32_e32 v73, v73
	v_rcp_f32_e32 v70, v70
	v_add_f32_e32 v71, 1.0, v71
	v_rcp_f32_e32 v71, v71
	v_add_f32_e32 v73, 1.0, v73
	v_rcp_f32_e32 v73, v73
	v_fma_mixlo_f16 v72, v66, v72, 0
	v_pk_mov_b32 v[66:67], v[66:67], v[68:69] op_sel:[1,0]
	v_pk_mul_f32 v[60:61], s[0:1], v[60:61] op_sel_hi:[0,1]
	v_pk_mul_f32 v[66:67], v[66:67], v[70:71]
	v_fma_mixlo_f16 v68, v69, v73, 0
	v_cvt_pk_f16_f32 v67, v66, v67
	v_pack_b32_f16 v66, v72, v67
	v_alignbit_b32 v67, v68, v67, 16
	v_lshl_add_u64 v[68:69], v[82:83], 0, v[114:115]
	global_store_dwordx2 v[68:69], v[66:67], off
	v_add_u32_e32 v66, 0x80, v132
	v_ashrrev_i32_e32 v66, 2, v66
	v_ashrrev_i32_e32 v67, 31, v66
	v_lshlrev_b64 v[66:67], 15, v[66:67]
	v_lshl_add_u64 v[66:67], s[2:3], 0, v[66:67]
	v_pk_mul_f32 v[58:59], s[0:1], v[58:59] op_sel_hi:[0,1]
	v_cvt_pk_f16_f32 v61, v60, v61
	v_cvt_pk_f16_f32 v60, v58, v59
	v_lshl_add_u64 v[58:59], v[66:67], 0, v[118:119]
	v_pk_mul_f32 v[54:55], s[0:1], v[54:55] op_sel_hi:[0,1]
	global_store_dwordx2 v[58:59], v[60:61], off
	v_mul_f32_e32 v58, 0xbfb8aa3b, v54
	v_exp_f32_e32 v58, v58
	v_mul_f32_e32 v59, 0xbfb8aa3b, v55
	v_exp_f32_e32 v59, v59
	v_pk_mul_f32 v[56:57], s[0:1], v[56:57] op_sel_hi:[0,1]
	v_add_f32_e32 v58, 1.0, v58
	v_rcp_f32_e32 v60, v58
	v_add_f32_e32 v58, 1.0, v59
	v_mul_f32_e32 v59, 0xbfb8aa3b, v56
	v_exp_f32_e32 v59, v59
	v_mul_f32_e32 v61, 0xbfb8aa3b, v57
	v_exp_f32_e32 v61, v61
	v_rcp_f32_e32 v58, v58
	v_add_f32_e32 v59, 1.0, v59
	v_rcp_f32_e32 v59, v59
	v_add_f32_e32 v61, 1.0, v61
	v_rcp_f32_e32 v61, v61
	v_fma_mixlo_f16 v60, v54, v60, 0
	v_pk_mov_b32 v[54:55], v[54:55], v[56:57] op_sel:[1,0]
	v_pk_mul_f32 v[80:81], s[0:1], v[80:81] op_sel_hi:[0,1]
	v_pk_mul_f32 v[54:55], v[54:55], v[58:59]
	v_pk_mul_f32 v[78:79], s[0:1], v[78:79] op_sel_hi:[0,1]
	v_cvt_pk_f16_f32 v55, v54, v55
	v_fma_mixlo_f16 v56, v57, v61, 0
	v_cvt_pk_f16_f32 v81, v80, v81
	v_cvt_pk_f16_f32 v80, v78, v79
	v_lshl_add_u64 v[78:79], v[82:83], 0, v[0:1]
	v_pack_b32_f16 v54, v60, v55
	v_alignbit_b32 v55, v56, v55, 16
	v_lshl_add_u64 v[56:57], v[66:67], 0, v[120:121]
	v_pk_mul_f32 v[50:51], s[0:1], v[50:51] op_sel_hi:[0,1]
	global_store_dwordx2 v[78:79], v[80:81], off
	global_store_dwordx2 v[56:57], v[54:55], off
	v_mul_f32_e32 v54, 0xbfb8aa3b, v50
	v_exp_f32_e32 v54, v54
	v_mul_f32_e32 v55, 0xbfb8aa3b, v51
	v_exp_f32_e32 v55, v55
	v_pk_mul_f32 v[52:53], s[0:1], v[52:53] op_sel_hi:[0,1]
	v_add_f32_e32 v54, 1.0, v54
	v_rcp_f32_e32 v56, v54
	v_add_f32_e32 v54, 1.0, v55
	v_mul_f32_e32 v55, 0xbfb8aa3b, v52
	v_exp_f32_e32 v55, v55
	v_mul_f32_e32 v57, 0xbfb8aa3b, v53
	v_exp_f32_e32 v57, v57
	v_rcp_f32_e32 v54, v54
	v_add_f32_e32 v55, 1.0, v55
	v_rcp_f32_e32 v55, v55
	v_add_f32_e32 v57, 1.0, v57
	v_rcp_f32_e32 v57, v57
	v_fma_mixlo_f16 v56, v50, v56, 0
	v_pk_mov_b32 v[50:51], v[50:51], v[52:53] op_sel:[1,0]
	v_pk_mul_f32 v[44:45], s[0:1], v[44:45] op_sel_hi:[0,1]
	v_pk_mul_f32 v[50:51], v[50:51], v[54:55]
	v_fma_mixlo_f16 v52, v53, v57, 0
	v_cvt_pk_f16_f32 v51, v50, v51
	v_pack_b32_f16 v50, v56, v51
	v_alignbit_b32 v51, v52, v51, 16
	v_lshl_add_u64 v[52:53], v[66:67], 0, v[114:115]
	global_store_dwordx2 v[52:53], v[50:51], off
	v_add_u32_e32 v50, 0x90, v132
	v_ashrrev_i32_e32 v50, 2, v50
	v_ashrrev_i32_e32 v51, 31, v50
	v_lshlrev_b64 v[50:51], 15, v[50:51]
	v_lshl_add_u64 v[50:51], s[2:3], 0, v[50:51]
	v_pk_mul_f32 v[42:43], s[0:1], v[42:43] op_sel_hi:[0,1]
	v_cvt_pk_f16_f32 v45, v44, v45
	v_cvt_pk_f16_f32 v44, v42, v43
	v_lshl_add_u64 v[42:43], v[50:51], 0, v[118:119]
	v_pk_mul_f32 v[38:39], s[0:1], v[38:39] op_sel_hi:[0,1]
	global_store_dwordx2 v[42:43], v[44:45], off
	v_mul_f32_e32 v42, 0xbfb8aa3b, v38
	v_exp_f32_e32 v42, v42
	v_mul_f32_e32 v43, 0xbfb8aa3b, v39
	v_exp_f32_e32 v43, v43
	v_pk_mul_f32 v[40:41], s[0:1], v[40:41] op_sel_hi:[0,1]
	v_add_f32_e32 v42, 1.0, v42
	v_rcp_f32_e32 v44, v42
	v_add_f32_e32 v42, 1.0, v43
	v_mul_f32_e32 v43, 0xbfb8aa3b, v40
	v_exp_f32_e32 v43, v43
	v_mul_f32_e32 v45, 0xbfb8aa3b, v41
	v_exp_f32_e32 v45, v45
	v_rcp_f32_e32 v42, v42
	v_add_f32_e32 v43, 1.0, v43
	v_rcp_f32_e32 v43, v43
	v_add_f32_e32 v45, 1.0, v45
	v_rcp_f32_e32 v45, v45
	v_fma_mixlo_f16 v44, v38, v44, 0
	v_pk_mov_b32 v[38:39], v[38:39], v[40:41] op_sel:[1,0]
	v_pk_mul_f32 v[64:65], s[0:1], v[64:65] op_sel_hi:[0,1]
	v_pk_mul_f32 v[38:39], v[38:39], v[42:43]
	v_pk_mul_f32 v[62:63], s[0:1], v[62:63] op_sel_hi:[0,1]
	v_cvt_pk_f16_f32 v39, v38, v39
	v_fma_mixlo_f16 v40, v41, v45, 0
	v_cvt_pk_f16_f32 v65, v64, v65
	v_cvt_pk_f16_f32 v64, v62, v63
	v_lshl_add_u64 v[62:63], v[66:67], 0, v[0:1]
	v_pack_b32_f16 v38, v44, v39
	v_alignbit_b32 v39, v40, v39, 16
	v_lshl_add_u64 v[40:41], v[50:51], 0, v[120:121]
	v_pk_mul_f32 v[34:35], s[0:1], v[34:35] op_sel_hi:[0,1]
	global_store_dwordx2 v[62:63], v[64:65], off
	global_store_dwordx2 v[40:41], v[38:39], off
	v_mul_f32_e32 v38, 0xbfb8aa3b, v34
	v_exp_f32_e32 v38, v38
	v_mul_f32_e32 v39, 0xbfb8aa3b, v35
	v_exp_f32_e32 v39, v39
	v_pk_mul_f32 v[36:37], s[0:1], v[36:37] op_sel_hi:[0,1]
	v_add_f32_e32 v38, 1.0, v38
	v_rcp_f32_e32 v40, v38
	v_add_f32_e32 v38, 1.0, v39
	v_mul_f32_e32 v39, 0xbfb8aa3b, v36
	v_exp_f32_e32 v39, v39
	v_mul_f32_e32 v41, 0xbfb8aa3b, v37
	v_exp_f32_e32 v41, v41
	v_rcp_f32_e32 v38, v38
	v_add_f32_e32 v39, 1.0, v39
	v_rcp_f32_e32 v39, v39
	v_add_f32_e32 v41, 1.0, v41
	v_rcp_f32_e32 v41, v41
	v_fma_mixlo_f16 v40, v34, v40, 0
	v_pk_mov_b32 v[34:35], v[34:35], v[36:37] op_sel:[1,0]
	v_pk_mul_f32 v[28:29], s[0:1], v[28:29] op_sel_hi:[0,1]
	v_pk_mul_f32 v[34:35], v[34:35], v[38:39]
	v_fma_mixlo_f16 v36, v37, v41, 0
	v_cvt_pk_f16_f32 v35, v34, v35
	v_pack_b32_f16 v34, v40, v35
	v_alignbit_b32 v35, v36, v35, 16
	v_lshl_add_u64 v[36:37], v[50:51], 0, v[114:115]
	global_store_dwordx2 v[36:37], v[34:35], off
	v_add_u32_e32 v34, 0xa0, v132
	v_ashrrev_i32_e32 v34, 2, v34
	v_ashrrev_i32_e32 v35, 31, v34
	v_lshlrev_b64 v[34:35], 15, v[34:35]
	v_lshl_add_u64 v[34:35], s[2:3], 0, v[34:35]
	v_pk_mul_f32 v[26:27], s[0:1], v[26:27] op_sel_hi:[0,1]
	v_cvt_pk_f16_f32 v29, v28, v29
	v_cvt_pk_f16_f32 v28, v26, v27
	v_lshl_add_u64 v[26:27], v[34:35], 0, v[118:119]
	v_pk_mul_f32 v[22:23], s[0:1], v[22:23] op_sel_hi:[0,1]
	global_store_dwordx2 v[26:27], v[28:29], off
	v_mul_f32_e32 v26, 0xbfb8aa3b, v22
	v_exp_f32_e32 v26, v26
	v_mul_f32_e32 v27, 0xbfb8aa3b, v23
	v_exp_f32_e32 v27, v27
	v_pk_mul_f32 v[24:25], s[0:1], v[24:25] op_sel_hi:[0,1]
	v_add_f32_e32 v26, 1.0, v26
	v_rcp_f32_e32 v28, v26
	v_add_f32_e32 v26, 1.0, v27
	v_mul_f32_e32 v27, 0xbfb8aa3b, v24
	v_exp_f32_e32 v27, v27
	v_mul_f32_e32 v29, 0xbfb8aa3b, v25
	v_exp_f32_e32 v29, v29
	v_rcp_f32_e32 v26, v26
	v_add_f32_e32 v27, 1.0, v27
	v_rcp_f32_e32 v27, v27
	v_add_f32_e32 v29, 1.0, v29
	v_rcp_f32_e32 v29, v29
	v_fma_mixlo_f16 v28, v22, v28, 0
	v_pk_mov_b32 v[22:23], v[22:23], v[24:25] op_sel:[1,0]
	v_pk_mul_f32 v[48:49], s[0:1], v[48:49] op_sel_hi:[0,1]
	v_pk_mul_f32 v[22:23], v[22:23], v[26:27]
	v_pk_mul_f32 v[46:47], s[0:1], v[46:47] op_sel_hi:[0,1]
	v_cvt_pk_f16_f32 v23, v22, v23
	v_fma_mixlo_f16 v24, v25, v29, 0
	v_cvt_pk_f16_f32 v49, v48, v49
	v_cvt_pk_f16_f32 v48, v46, v47
	v_lshl_add_u64 v[46:47], v[50:51], 0, v[0:1]
	v_pack_b32_f16 v22, v28, v23
	v_alignbit_b32 v23, v24, v23, 16
	v_lshl_add_u64 v[24:25], v[34:35], 0, v[120:121]
	v_pk_mul_f32 v[18:19], s[0:1], v[18:19] op_sel_hi:[0,1]
	global_store_dwordx2 v[46:47], v[48:49], off
	global_store_dwordx2 v[24:25], v[22:23], off
	v_mul_f32_e32 v22, 0xbfb8aa3b, v18
	v_exp_f32_e32 v22, v22
	v_mul_f32_e32 v23, 0xbfb8aa3b, v19
	v_exp_f32_e32 v23, v23
	v_pk_mul_f32 v[20:21], s[0:1], v[20:21] op_sel_hi:[0,1]
	v_add_f32_e32 v22, 1.0, v22
	v_rcp_f32_e32 v24, v22
	v_add_f32_e32 v22, 1.0, v23
	v_mul_f32_e32 v23, 0xbfb8aa3b, v20
	v_exp_f32_e32 v23, v23
	v_mul_f32_e32 v25, 0xbfb8aa3b, v21
	v_exp_f32_e32 v25, v25
	v_rcp_f32_e32 v22, v22
	v_add_f32_e32 v23, 1.0, v23
	v_rcp_f32_e32 v23, v23
	v_add_f32_e32 v25, 1.0, v25
	v_rcp_f32_e32 v25, v25
	v_fma_mixlo_f16 v24, v18, v24, 0
	v_pk_mov_b32 v[18:19], v[18:19], v[20:21] op_sel:[1,0]
	v_pk_mul_f32 v[32:33], s[0:1], v[32:33] op_sel_hi:[0,1]
	v_pk_mul_f32 v[18:19], v[18:19], v[22:23]
	v_fma_mixlo_f16 v20, v21, v25, 0
	v_cvt_pk_f16_f32 v19, v18, v19
	v_pack_b32_f16 v18, v24, v19
	v_alignbit_b32 v19, v20, v19, 16
	v_lshl_add_u64 v[20:21], v[34:35], 0, v[114:115]
	global_store_dwordx2 v[20:21], v[18:19], off
	v_add_u32_e32 v18, 0xb0, v132
	v_ashrrev_i32_e32 v18, 2, v18
	v_ashrrev_i32_e32 v19, 31, v18
	v_lshlrev_b64 v[18:19], 15, v[18:19]
	v_pk_mul_f32 v[30:31], s[0:1], v[30:31] op_sel_hi:[0,1]
	v_lshl_add_u64 v[18:19], s[2:3], 0, v[18:19]
	v_pk_mul_f32 v[16:17], s[0:1], v[16:17] op_sel_hi:[0,1]
	v_pk_mul_f32 v[14:15], s[0:1], v[14:15] op_sel_hi:[0,1]
	v_cvt_pk_f16_f32 v33, v32, v33
	v_cvt_pk_f16_f32 v32, v30, v31
	v_lshl_add_u64 v[30:31], v[34:35], 0, v[0:1]
	v_cvt_pk_f16_f32 v17, v16, v17
	v_cvt_pk_f16_f32 v16, v14, v15
	v_lshl_add_u64 v[0:1], v[18:19], 0, v[0:1]
	global_store_dwordx2 v[0:1], v[16:17], off
	v_pk_mul_f32 v[0:1], s[0:1], v[12:13] op_sel_hi:[0,1]
	v_pk_mul_f32 v[10:11], s[0:1], v[10:11] op_sel_hi:[0,1]
	v_cvt_pk_f16_f32 v1, v0, v1
	v_cvt_pk_f16_f32 v0, v10, v11
	v_lshl_add_u64 v[10:11], v[18:19], 0, v[118:119]
	global_store_dwordx2 v[10:11], v[0:1], off
	v_pk_mul_f32 v[0:1], s[0:1], v[6:7] op_sel_hi:[0,1]
	v_mul_f32_e32 v6, 0xbfb8aa3b, v0
	v_exp_f32_e32 v10, v6
	v_mul_f32_e32 v6, 0xbfb8aa3b, v1
	v_exp_f32_e32 v11, v6
	v_pk_mul_f32 v[6:7], s[0:1], v[8:9] op_sel_hi:[0,1]
	v_add_f32_e32 v8, 1.0, v10
	v_mul_f32_e32 v9, 0xbfb8aa3b, v6
	v_rcp_f32_e32 v10, v8
	v_add_f32_e32 v8, 1.0, v11
	v_exp_f32_e32 v9, v9
	v_mul_f32_e32 v11, 0xbfb8aa3b, v7
	v_exp_f32_e32 v11, v11
	v_rcp_f32_e32 v8, v8
	v_add_f32_e32 v9, 1.0, v9
	v_rcp_f32_e32 v9, v9
	v_add_f32_e32 v11, 1.0, v11
	v_rcp_f32_e32 v11, v11
	v_fma_mixlo_f16 v10, v0, v10, 0
	v_pk_mov_b32 v[0:1], v[0:1], v[6:7] op_sel:[1,0]
	global_store_dwordx2 v[30:31], v[32:33], off
	v_pk_mul_f32 v[0:1], v[0:1], v[8:9]
	v_fma_mixlo_f16 v6, v7, v11, 0
	v_cvt_pk_f16_f32 v1, v0, v1
	v_pack_b32_f16 v0, v10, v1
	v_alignbit_b32 v1, v6, v1, 16
	v_lshl_add_u64 v[6:7], v[18:19], 0, v[120:121]
	global_store_dwordx2 v[6:7], v[0:1], off
	v_pk_mul_f32 v[0:1], s[0:1], v[2:3] op_sel_hi:[0,1]
	v_mul_f32_e32 v2, 0xbfb8aa3b, v0
	v_exp_f32_e32 v6, v2
	v_mul_f32_e32 v2, 0xbfb8aa3b, v1
	v_exp_f32_e32 v7, v2
	v_pk_mul_f32 v[2:3], s[0:1], v[4:5] op_sel_hi:[0,1]
	v_add_f32_e32 v4, 1.0, v6
	v_mul_f32_e32 v5, 0xbfb8aa3b, v2
	v_rcp_f32_e32 v6, v4
	v_add_f32_e32 v4, 1.0, v7
	v_exp_f32_e32 v5, v5
	v_mul_f32_e32 v7, 0xbfb8aa3b, v3
	v_exp_f32_e32 v7, v7
	v_rcp_f32_e32 v4, v4
	v_add_f32_e32 v5, 1.0, v5
	v_rcp_f32_e32 v5, v5
	v_add_f32_e32 v7, 1.0, v7
	v_rcp_f32_e32 v7, v7
	v_fma_mixlo_f16 v6, v0, v6, 0
	v_pk_mov_b32 v[0:1], v[0:1], v[2:3] op_sel:[1,0]
	v_fma_mixlo_f16 v2, v3, v7, 0
	v_pk_mul_f32 v[0:1], v[0:1], v[4:5]
	s_nop 0
	v_cvt_pk_f16_f32 v1, v0, v1
	v_pack_b32_f16 v0, v6, v1
	v_alignbit_b32 v1, v2, v1, 16
	v_lshl_add_u64 v[2:3], v[18:19], 0, v[114:115]
	global_store_dwordx2 v[2:3], v[0:1], off
	s_endpgm
	.p2alignl 8, 3212836864

	.amdhsa_kernel _Z11gemm_8phaseILi0ELi16ELi16ELi1024ELi1024ELi4096ELi1EEvPKDF16_S1_PvS2_fPj
		.amdhsa_group_segment_fixed_size 0
		.amdhsa_private_segment_fixed_size 0
		.amdhsa_kernarg_size 48
		.amdhsa_user_sgpr_count 2
		.amdhsa_user_sgpr_dispatch_ptr 0
		.amdhsa_user_sgpr_queue_ptr 0
		.amdhsa_user_sgpr_kernarg_segment_ptr 1
		.amdhsa_user_sgpr_dispatch_id 0
		.amdhsa_user_sgpr_kernarg_preload_length 0
		.amdhsa_user_sgpr_kernarg_preload_offset 0
		.amdhsa_user_sgpr_private_segment_size 0
		.amdhsa_uses_dynamic_stack 0
		.amdhsa_enable_private_segment 0
		.amdhsa_system_sgpr_workgroup_id_x 1
		.amdhsa_system_sgpr_workgroup_id_y 0
		.amdhsa_system_sgpr_workgroup_id_z 0
		.amdhsa_system_sgpr_workgroup_info 0
		.amdhsa_system_vgpr_workitem_id 0
		.amdhsa_next_free_vgpr 236
		.amdhsa_next_free_sgpr 34
		.amdhsa_accum_offset 236
		.amdhsa_reserve_vcc 1
		.amdhsa_float_round_mode_32 0
		.amdhsa_float_round_mode_16_64 0
		.amdhsa_float_denorm_mode_32 3
		.amdhsa_float_denorm_mode_16_64 3
		.amdhsa_dx10_clamp 1
		.amdhsa_ieee_mode 1
		.amdhsa_fp16_overflow 0
		.amdhsa_tg_split 0
		.amdhsa_exception_fp_ieee_invalid_op 0
		.amdhsa_exception_fp_denorm_src 0
		.amdhsa_exception_fp_ieee_div_zero 0
		.amdhsa_exception_fp_ieee_overflow 0
		.amdhsa_exception_fp_ieee_underflow 0
		.amdhsa_exception_fp_ieee_inexact 0
		.amdhsa_exception_int_div_zero 0
	.end_amdhsa_kernel

_Z11gemm_8phaseILi2ELi16ELi4ELi512ELi2048ELi1024ELi4EEvPKDF16_S1_PvS2_fPj:
	s_and_b32 s3, s2, 7
	s_lshr_b32 s4, s2, 3
	s_and_b32 s9, s4, 3
	s_lshl_b32 s3, s3, 2
	s_add_i32 s3, s3, s9
	s_lshl_b32 s33, s3, 7
	s_lshr_b32 s4, s4, 2
	s_lshl_b32 s8, s4, 7
	v_lshrrev_b32_e32 v3, 3, v0
	v_and_b32_e32 v4, 48, v3
	v_bfe_u32 v5, v0, 2, 4
	v_and_b32_e32 v2, 32, v0
	v_or_b32_e32 v10, v4, v5
	s_load_dword s34, s[0:1], 0x20
	s_load_dwordx2 s[36:37], s[0:1], 0x10
	v_lshlrev_b32_e32 v1, 4, v0
	s_load_dwordx4 s[4:7], s[0:1], 0x0
	v_bitop3_b32 v6, v1, v2, 48 bitop3:0x6c
	v_or_b32_e32 v2, s8, v10
	v_ashrrev_i32_e32 v3, 31, v2
	v_mov_b32_e32 v131, 0
	v_lshlrev_b64 v[8:9], 12, v[2:3]
	v_or_b32_e32 v2, s33, v10
	v_mov_b32_e32 v3, v131
	v_and_b32_e32 v7, 64, v0
	v_lshlrev_b64 v[2:3], 12, v[2:3]
	s_add_i32 s22, 0, 0x10000
	v_or_b32_e32 v130, v6, v7
	s_waitcnt lgkmcnt(0)
	v_lshl_add_u64 v[2:3], s[4:5], 0, v[2:3]
	v_add_u32_e32 v145, s22, v1
	s_mov_b32 s21, 0
	v_lshl_add_u64 v[2:3], v[2:3], 0, v[130:131]
	s_mov_b32 s20, 0
	v_readfirstlane_b32 s10, v145
	v_add_u32_e32 v146, 0x2000, v145
	v_lshl_add_u64 v[8:9], s[6:7], 0, v[8:9]
	v_lshl_add_u64 v[2:3], v[2:3], 0, s[20:21]
	s_mov_b32 m0, s10
	s_mov_b64 s[10:11], 0x40000
	v_readfirstlane_b32 s12, v146
	v_lshl_add_u64 v[8:9], v[8:9], 0, v[130:131]
	v_add_u32_e32 v142, 0, v1
	global_load_lds_dwordx4 v[2:3], off
	v_lshl_add_u64 v[10:11], v[2:3], 0, s[10:11]
	s_mov_b32 m0, s12
	v_lshl_add_u64 v[132:133], v[8:9], 0, s[20:21]
	v_readfirstlane_b32 s12, v142
	v_add_u32_e32 v147, 0x2000, v142
	s_add_i32 s21, 0, 0x14000
	global_load_lds_dwordx4 v[10:11], off
	s_mov_b32 m0, s12
	v_lshl_add_u64 v[8:9], v[132:133], 0, s[10:11]
	v_readfirstlane_b32 s10, v147
	v_add_u32_e32 v150, s21, v1
	global_load_lds_dwordx4 v[132:133], off
	s_mov_b32 m0, s10
	s_mov_b64 s[10:11], 0x800
	v_readfirstlane_b32 s12, v150
	v_add_u32_e32 v152, 0x2000, v150
	global_load_lds_dwordx4 v[8:9], off
	v_lshl_add_u64 v[8:9], v[2:3], 0, s[10:11]
	s_mov_b32 m0, s12
	s_mov_b64 s[12:13], 0x40800
	v_readfirstlane_b32 s16, v152
	global_load_lds_dwordx4 v[8:9], off
	v_lshl_add_u64 v[8:9], v[2:3], 0, s[12:13]
	s_mov_b32 m0, s16
	v_add_u32_e32 v153, 0x4000, v142
	global_load_lds_dwordx4 v[8:9], off
	v_lshl_add_u64 v[8:9], v[132:133], 0, s[10:11]
	v_readfirstlane_b32 s10, v153
	v_add_u32_e32 v154, 0x6000, v142
	s_mov_b32 m0, s10
	v_readfirstlane_b32 s10, v154
	global_load_lds_dwordx4 v[8:9], off
	v_lshl_add_u64 v[8:9], v[132:133], 0, s[12:13]
	s_mov_b32 m0, s10
	global_load_lds_dwordx4 v[8:9], off
	v_lshrrev_b32_e32 v8, 8, v0
	v_cmp_eq_u32_e32 vcc, 1, v8
	s_and_saveexec_b64 s[10:11], vcc
	s_cbranch_execz .LBB7_2
	s_barrier

.Lop_deskew:
	s_or_b64 exec, exec, s[4:5]
	v_lshl_add_u64 v[230:231], v[136:137], 0, v[130:131]
	v_readfirstlane_b32 s9, v163
	v_lshl_add_u64 v[182:183], v[230:231], 0, s[16:17]
	s_mov_b32 m0, s9
	v_readfirstlane_b32 s9, v164
	global_load_lds_dwordx4 v[182:183], off
	v_lshl_add_u64 v[182:183], v[230:231], 0, s[18:19]
	s_mov_b32 m0, s9
	s_nop 0
	global_load_lds_dwordx4 v[182:183], off
	ds_read_b128 v[166:169], v162
	ds_read_b128 v[170:173], v162 offset:1024
	ds_read_b128 v[174:177], v162 offset:2048
	ds_read_b128 v[178:181], v162 offset:3072
	ds_read_b128 v[182:185], v141
	ds_read_b128 v[186:189], v141 offset:1024
	ds_read_b128 v[190:193], v140
	ds_read_b128 v[194:197], v140 offset:1024
	ds_read_b128 v[198:201], v139
	ds_read_b128 v[202:205], v139 offset:1024
	ds_read_b128 v[206:209], v138
	ds_read_b128 v[210:213], v138 offset:1024
	s_waitcnt lgkmcnt(0)
	v_mfma_f32_16x16x32_f16 v[126:129], v[182:185], v[166:169], v[126:129]
	v_mfma_f32_16x16x32_f16 v[122:125], v[182:185], v[174:177], v[122:125]
	v_mfma_f32_16x16x32_f16 v[118:121], v[190:193], v[166:169], v[118:121]
	v_mfma_f32_16x16x32_f16 v[114:117], v[190:193], v[174:177], v[114:117]
	v_mfma_f32_16x16x32_f16 v[110:113], v[198:201], v[166:169], v[110:113]
	v_mfma_f32_16x16x32_f16 v[106:109], v[198:201], v[174:177], v[106:109]
	v_mfma_f32_16x16x32_f16 v[102:105], v[206:209], v[166:169], v[102:105]
	v_mfma_f32_16x16x32_f16 v[98:101], v[206:209], v[174:177], v[98:101]
	v_mfma_f32_16x16x32_f16 v[126:129], v[186:189], v[170:173], v[126:129]
	v_mfma_f32_16x16x32_f16 v[122:125], v[186:189], v[178:181], v[122:125]
	v_mfma_f32_16x16x32_f16 v[118:121], v[194:197], v[170:173], v[118:121]
	v_mfma_f32_16x16x32_f16 v[114:117], v[194:197], v[178:181], v[114:117]
	v_mfma_f32_16x16x32_f16 v[110:113], v[202:205], v[170:173], v[110:113]
	v_mfma_f32_16x16x32_f16 v[106:109], v[202:205], v[178:181], v[106:109]
	v_mfma_f32_16x16x32_f16 v[102:105], v[210:213], v[170:173], v[102:105]
	v_mfma_f32_16x16x32_f16 v[98:101], v[210:213], v[178:181], v[98:101]
	s_nop 7
	ds_read_b128 v[214:217], v160
	ds_read_b128 v[218:221], v160 offset:1024
	ds_read_b128 v[222:225], v160 offset:2048
	ds_read_b128 v[226:229], v160 offset:3072
	ds_read_b128 v[182:185], v141 offset:16384
	ds_read_b128 v[186:189], v141 offset:17408
	ds_read_b128 v[190:193], v140 offset:16384
	ds_read_b128 v[194:197], v140 offset:17408
	ds_read_b128 v[198:201], v139 offset:16384
	ds_read_b128 v[202:205], v139 offset:17408
	ds_read_b128 v[206:209], v138 offset:16384
	ds_read_b128 v[210:213], v138 offset:17408
	s_waitcnt lgkmcnt(0)
	v_mfma_f32_16x16x32_f16 v[30:33], v[182:185], v[214:217], v[30:33]
	v_mfma_f32_16x16x32_f16 v[26:29], v[182:185], v[222:225], v[26:29]
	v_mfma_f32_16x16x32_f16 v[22:25], v[190:193], v[214:217], v[22:25]
	v_mfma_f32_16x16x32_f16 v[18:21], v[190:193], v[222:225], v[18:21]
	v_mfma_f32_16x16x32_f16 v[14:17], v[198:201], v[214:217], v[14:17]
	v_mfma_f32_16x16x32_f16 v[10:13], v[198:201], v[222:225], v[10:13]
	v_mfma_f32_16x16x32_f16 v[6:9], v[206:209], v[214:217], v[6:9]
	v_mfma_f32_16x16x32_f16 v[2:5], v[206:209], v[222:225], v[2:5]
	v_mfma_f32_16x16x32_f16 v[30:33], v[186:189], v[218:221], v[30:33]
	v_mfma_f32_16x16x32_f16 v[26:29], v[186:189], v[226:229], v[26:29]
	v_mfma_f32_16x16x32_f16 v[22:25], v[194:197], v[218:221], v[22:25]
	v_mfma_f32_16x16x32_f16 v[18:21], v[194:197], v[226:229], v[18:21]
	v_mfma_f32_16x16x32_f16 v[14:17], v[202:205], v[218:221], v[14:17]
	v_mfma_f32_16x16x32_f16 v[10:13], v[202:205], v[226:229], v[10:13]
	v_mfma_f32_16x16x32_f16 v[6:9], v[210:213], v[218:221], v[6:9]
	v_mfma_f32_16x16x32_f16 v[2:5], v[210:213], v[226:229], v[2:5]
	s_nop 7
	s_waitcnt vmcnt(0)
	s_barrier
	ds_read_b128 v[166:169], v151
	ds_read_b128 v[170:173], v151 offset:1024
	ds_read_b128 v[174:177], v151 offset:2048
	ds_read_b128 v[178:181], v151 offset:3072
	ds_read_b128 v[182:185], v141 offset:32768
	ds_read_b128 v[186:189], v141 offset:33792
	ds_read_b128 v[190:193], v140 offset:32768
	ds_read_b128 v[194:197], v140 offset:33792
	ds_read_b128 v[198:201], v139 offset:32768
	ds_read_b128 v[202:205], v139 offset:33792
	ds_read_b128 v[206:209], v138 offset:32768
	ds_read_b128 v[210:213], v138 offset:33792
	s_waitcnt lgkmcnt(0)
	v_mfma_f32_16x16x32_f16 v[126:129], v[182:185], v[166:169], v[126:129]
	v_mfma_f32_16x16x32_f16 v[122:125], v[182:185], v[174:177], v[122:125]
	v_mfma_f32_16x16x32_f16 v[118:121], v[190:193], v[166:169], v[118:121]
	v_mfma_f32_16x16x32_f16 v[114:117], v[190:193], v[174:177], v[114:117]
	v_mfma_f32_16x16x32_f16 v[110:113], v[198:201], v[166:169], v[110:113]
	v_mfma_f32_16x16x32_f16 v[106:109], v[198:201], v[174:177], v[106:109]
	v_mfma_f32_16x16x32_f16 v[102:105], v[206:209], v[166:169], v[102:105]
	v_mfma_f32_16x16x32_f16 v[98:101], v[206:209], v[174:177], v[98:101]
	v_mfma_f32_16x16x32_f16 v[126:129], v[186:189], v[170:173], v[126:129]
	v_mfma_f32_16x16x32_f16 v[122:125], v[186:189], v[178:181], v[122:125]
	v_mfma_f32_16x16x32_f16 v[118:121], v[194:197], v[170:173], v[118:121]
	v_mfma_f32_16x16x32_f16 v[114:117], v[194:197], v[178:181], v[114:117]
	v_mfma_f32_16x16x32_f16 v[110:113], v[202:205], v[170:173], v[110:113]
	v_mfma_f32_16x16x32_f16 v[106:109], v[202:205], v[178:181], v[106:109]
	v_mfma_f32_16x16x32_f16 v[102:105], v[210:213], v[170:173], v[102:105]
	v_mfma_f32_16x16x32_f16 v[98:101], v[210:213], v[178:181], v[98:101]
	s_nop 7
	ds_read_b128 v[214:217], v144
	ds_read_b128 v[218:221], v144 offset:1024
	ds_read_b128 v[222:225], v144 offset:2048
	ds_read_b128 v[226:229], v144 offset:3072
	ds_read_b128 v[182:185], v141 offset:49152
	ds_read_b128 v[186:189], v141 offset:50176
	ds_read_b128 v[190:193], v140 offset:49152
	ds_read_b128 v[194:197], v140 offset:50176
	ds_read_b128 v[198:201], v139 offset:49152
	ds_read_b128 v[202:205], v139 offset:50176
	ds_read_b128 v[206:209], v138 offset:49152
	ds_read_b128 v[210:213], v138 offset:50176
	s_waitcnt lgkmcnt(0)
	v_mfma_f32_16x16x32_f16 v[30:33], v[182:185], v[214:217], v[30:33]
	v_mfma_f32_16x16x32_f16 v[26:29], v[182:185], v[222:225], v[26:29]
	v_mfma_f32_16x16x32_f16 v[22:25], v[190:193], v[214:217], v[22:25]
	v_mfma_f32_16x16x32_f16 v[18:21], v[190:193], v[222:225], v[18:21]
	v_mfma_f32_16x16x32_f16 v[14:17], v[198:201], v[214:217], v[14:17]
	v_mfma_f32_16x16x32_f16 v[10:13], v[198:201], v[222:225], v[10:13]
	v_mfma_f32_16x16x32_f16 v[6:9], v[206:209], v[214:217], v[6:9]
	v_mfma_f32_16x16x32_f16 v[2:5], v[206:209], v[222:225], v[2:5]
	v_mfma_f32_16x16x32_f16 v[30:33], v[186:189], v[218:221], v[30:33]
	v_mfma_f32_16x16x32_f16 v[26:29], v[186:189], v[226:229], v[26:29]
	v_mfma_f32_16x16x32_f16 v[22:25], v[194:197], v[218:221], v[22:25]
	v_mfma_f32_16x16x32_f16 v[18:21], v[194:197], v[226:229], v[18:21]
	v_mfma_f32_16x16x32_f16 v[14:17], v[202:205], v[218:221], v[14:17]
	v_mfma_f32_16x16x32_f16 v[10:13], v[202:205], v[226:229], v[10:13]
	v_mfma_f32_16x16x32_f16 v[6:9], v[210:213], v[218:221], v[6:9]
	v_mfma_f32_16x16x32_f16 v[2:5], v[210:213], v[226:229], v[2:5]
	v_and_b32_e32 v130, 15, v0
	v_bfe_u32 v131, v0, 6, 2
	v_lshl_add_u32 v130, v131, 5, v130
	v_add_u32_e32 v130, s33, v130
	v_bfe_u32 v131, v0, 4, 2
	v_lshrrev_b32_e32 v132, 8, v0
	v_lshlrev_b32_e32 v131, 2, v131
	v_lshl_add_u32 v131, v132, 6, v131
	v_add_u32_e32 v131, s8, v131
	v_lshlrev_b32_e32 v131, 2, v131
	v_lshl_add_u32 v130, v130, 12, v131
	v_mov_b32_e32 v131, 0
	s_mov_b64 s[4:5], 0x10000
	s_waitcnt lgkmcnt(0)
	v_lshl_add_u64 v[130:131], s[36:37], 0, v[130:131]
	v_lshl_add_u64 v[132:133], v[130:131], 0, s[4:5]
	s_nop 7
	s_nop 7
	v_pk_add_f32 v[126:127], v[126:127], v[30:31]
	v_pk_add_f32 v[128:129], v[128:129], v[32:33]
	v_pk_mul_f32 v[126:127], v[126:127], s[34:35] op_sel_hi:[1,0]
	v_pk_mul_f32 v[128:129], v[128:129], s[34:35] op_sel_hi:[1,0]
	global_store_dwordx4 v[130:131], v[126:129], off nt
	v_pk_add_f32 v[122:123], v[122:123], v[26:27]
	v_pk_add_f32 v[124:125], v[124:125], v[28:29]
	v_pk_mul_f32 v[122:123], v[122:123], s[34:35] op_sel_hi:[1,0]
	v_pk_mul_f32 v[124:125], v[124:125], s[34:35] op_sel_hi:[1,0]
	global_store_dwordx4 v[132:133], v[122:125], off nt
	v_pk_add_f32 v[118:119], v[118:119], v[22:23]
	v_pk_add_f32 v[120:121], v[120:121], v[24:25]
	v_pk_mul_f32 v[118:119], v[118:119], s[34:35] op_sel_hi:[1,0]
	v_pk_mul_f32 v[120:121], v[120:121], s[34:35] op_sel_hi:[1,0]
	global_store_dwordx4 v[130:131], v[118:121], off offset:64 nt
	v_pk_add_f32 v[114:115], v[114:115], v[18:19]
	v_pk_add_f32 v[116:117], v[116:117], v[20:21]
	v_pk_mul_f32 v[114:115], v[114:115], s[34:35] op_sel_hi:[1,0]
	v_pk_mul_f32 v[116:117], v[116:117], s[34:35] op_sel_hi:[1,0]
	global_store_dwordx4 v[132:133], v[114:117], off offset:64 nt
	v_pk_add_f32 v[110:111], v[110:111], v[14:15]
	v_pk_add_f32 v[112:113], v[112:113], v[16:17]
	v_pk_mul_f32 v[110:111], v[110:111], s[34:35] op_sel_hi:[1,0]
	v_pk_mul_f32 v[112:113], v[112:113], s[34:35] op_sel_hi:[1,0]
	global_store_dwordx4 v[130:131], v[110:113], off offset:128 nt
	v_pk_add_f32 v[106:107], v[106:107], v[10:11]
	v_pk_add_f32 v[108:109], v[108:109], v[12:13]
	v_pk_mul_f32 v[106:107], v[106:107], s[34:35] op_sel_hi:[1,0]
	v_pk_mul_f32 v[108:109], v[108:109], s[34:35] op_sel_hi:[1,0]
	global_store_dwordx4 v[132:133], v[106:109], off offset:128 nt
	v_pk_add_f32 v[102:103], v[102:103], v[6:7]
	v_pk_add_f32 v[104:105], v[104:105], v[8:9]
	v_pk_mul_f32 v[102:103], v[102:103], s[34:35] op_sel_hi:[1,0]
	v_pk_mul_f32 v[104:105], v[104:105], s[34:35] op_sel_hi:[1,0]
	global_store_dwordx4 v[130:131], v[102:105], off offset:192 nt
	v_pk_add_f32 v[98:99], v[98:99], v[2:3]
	v_pk_add_f32 v[100:101], v[100:101], v[4:5]
	v_pk_mul_f32 v[98:99], v[98:99], s[34:35] op_sel_hi:[1,0]
	v_pk_mul_f32 v[100:101], v[100:101], s[34:35] op_sel_hi:[1,0]
	global_store_dwordx4 v[132:133], v[98:101], off offset:192 nt
	s_endpgm
	.p2alignl 8, 3212836864

	.amdhsa_kernel _Z11gemm_8phaseILi2ELi16ELi4ELi512ELi2048ELi1024ELi4EEvPKDF16_S1_PvS2_fPj
		.amdhsa_group_segment_fixed_size 0
		.amdhsa_private_segment_fixed_size 0
		.amdhsa_kernarg_size 48
		.amdhsa_user_sgpr_count 2
		.amdhsa_user_sgpr_dispatch_ptr 0
		.amdhsa_user_sgpr_queue_ptr 0
		.amdhsa_user_sgpr_kernarg_segment_ptr 1
		.amdhsa_user_sgpr_dispatch_id 0
		.amdhsa_user_sgpr_kernarg_preload_length 0
		.amdhsa_user_sgpr_kernarg_preload_offset 0
		.amdhsa_user_sgpr_private_segment_size 0
		.amdhsa_uses_dynamic_stack 0
		.amdhsa_enable_private_segment 0
		.amdhsa_system_sgpr_workgroup_id_x 1
		.amdhsa_system_sgpr_workgroup_id_y 0
		.amdhsa_system_sgpr_workgroup_id_z 0
		.amdhsa_system_sgpr_workgroup_info 0
		.amdhsa_system_vgpr_workitem_id 0
		.amdhsa_next_free_vgpr 236
		.amdhsa_next_free_sgpr 38
		.amdhsa_accum_offset 236
		.amdhsa_reserve_vcc 1
		.amdhsa_float_round_mode_32 0
		.amdhsa_float_round_mode_16_64 0
		.amdhsa_float_denorm_mode_32 3
		.amdhsa_float_denorm_mode_16_64 3
		.amdhsa_dx10_clamp 1
		.amdhsa_ieee_mode 1
		.amdhsa_fp16_overflow 0
		.amdhsa_tg_split 0
		.amdhsa_exception_fp_ieee_invalid_op 0
		.amdhsa_exception_fp_denorm_src 0
		.amdhsa_exception_fp_ieee_div_zero 0
		.amdhsa_exception_fp_ieee_overflow 0
		.amdhsa_exception_fp_ieee_underflow 0
		.amdhsa_exception_fp_ieee_inexact 0
		.amdhsa_exception_int_div_zero 0
	.end_amdhsa_kernel

amdhsa.kernels:
  - .agpr_count:     0
    .args:
      - .address_space:  global
        .offset:         0
        .size:           8
        .value_kind:     global_buffer
      - .address_space:  global
        .offset:         8
        .size:           8
        .value_kind:     global_buffer
      - .offset:         16
        .size:           8
        .value_kind:     by_value
      - .address_space:  global
        .offset:         24
        .size:           8
        .value_kind:     global_buffer
      - .address_space:  global
        .offset:         32
        .size:           8
        .value_kind:     global_buffer
      - .offset:         40
        .size:           8
        .value_kind:     by_value
      - .address_space:  global
        .offset:         48
        .size:           8
        .value_kind:     global_buffer
      - .address_space:  global
        .offset:         56
        .size:           8
        .value_kind:     global_buffer
      - .offset:         64
        .size:           8
        .value_kind:     by_value
      - .address_space:  global
        .offset:         72
        .size:           8
        .value_kind:     global_buffer
      - .address_space:  global
        .offset:         80
        .size:           8
        .value_kind:     global_buffer
      - .offset:         88
        .size:           8
        .value_kind:     by_value
      - .address_space:  global
        .offset:         96
        .size:           8
        .value_kind:     global_buffer
      - .address_space:  global
        .offset:         104
        .size:           8
        .value_kind:     global_buffer
      - .offset:         112
        .size:           8
        .value_kind:     by_value
      - .address_space:  global
        .offset:         120
        .size:           8
        .value_kind:     global_buffer
      - .actual_access:  read_only
        .address_space:  global
        .offset:         128
        .size:           8
        .value_kind:     global_buffer
      - .actual_access:  write_only
        .address_space:  global
        .offset:         136
        .size:           8
        .value_kind:     global_buffer
    .group_segment_fixed_size: 0
    .kernarg_segment_align: 8
    .kernarg_segment_size: 144
    .language:       OpenCL C
    .language_version:
      - 2
      - 0
    .max_flat_workgroup_size: 256
    .name:           _Z10cvt_kernelPKfPDF16_lS0_S1_lS0_S1_lS0_S1_lS0_S1_lPjS0_Pf
    .private_segment_fixed_size: 0
    .sgpr_count:     58
    .sgpr_spill_count: 0
    .symbol:         _Z10cvt_kernelPKfPDF16_lS0_S1_lS0_S1_lS0_S1_lS0_S1_lPjS0_Pf.kd
    .uniform_work_group_size: 1
    .uses_dynamic_stack: false
    .vgpr_count:     18
    .vgpr_spill_count: 0
    .wavefront_size: 64
  - .agpr_count:     0
    .args:
      - .actual_access:  read_only
        .address_space:  global
        .offset:         0
        .size:           8
        .value_kind:     global_buffer
      - .actual_access:  read_only
        .address_space:  global
        .offset:         8
        .size:           8
        .value_kind:     global_buffer
      - .actual_access:  read_only
        .address_space:  global
        .offset:         16
        .size:           8
        .value_kind:     global_buffer
      - .actual_access:  read_only
        .address_space:  global
        .offset:         24
        .size:           8
        .value_kind:     global_buffer
      - .actual_access:  write_only
        .address_space:  global
        .offset:         32
        .size:           8
        .value_kind:     global_buffer
      - .actual_access:  write_only
        .address_space:  global
        .offset:         40
        .size:           8
        .value_kind:     global_buffer
      - .actual_access:  write_only
        .address_space:  global
        .offset:         48
        .size:           8
        .value_kind:     global_buffer
    .group_segment_fixed_size: 65792
    .kernarg_segment_align: 8
    .kernarg_segment_size: 56
    .language:       OpenCL C
    .language_version:
      - 2
      - 0
    .max_flat_workgroup_size: 1024
    .name:           _Z17conv_xproj_kernelPKDF16_PKfS2_S0_PDF16_S3_Pf
    .private_segment_fixed_size: 0
    .sgpr_count:     30
    .sgpr_spill_count: 0
    .symbol:         _Z17conv_xproj_kernelPKDF16_PKfS2_S0_PDF16_S3_Pf.kd
    .uniform_work_group_size: 1
    .uses_dynamic_stack: false
    .vgpr_count:     128
    .vgpr_spill_count: 0
    .wavefront_size: 64
  - .agpr_count:     0
    .args:
      - .actual_access:  read_only
        .address_space:  global
        .offset:         0
        .size:           8
        .value_kind:     global_buffer
      - .actual_access:  read_only
        .address_space:  global
        .offset:         8
        .size:           8
        .value_kind:     global_buffer
      - .actual_access:  read_only
        .address_space:  global
        .offset:         16
        .size:           8
        .value_kind:     global_buffer
      - .actual_access:  read_only
        .address_space:  global
        .offset:         24
        .size:           8
        .value_kind:     global_buffer
      - .actual_access:  read_only
        .address_space:  global
        .offset:         32
        .size:           8
        .value_kind:     global_buffer
      - .actual_access:  read_only
        .address_space:  global
        .offset:         40
        .size:           8
        .value_kind:     global_buffer
      - .actual_access:  write_only
        .address_space:  global
        .offset:         48
        .size:           8
        .value_kind:     global_buffer
      - .actual_access:  write_only
        .address_space:  global
        .offset:         56
        .size:           8
        .value_kind:     global_buffer
      - .actual_access:  write_only
        .address_space:  global
        .offset:         64
        .size:           8
        .value_kind:     global_buffer
      - .actual_access:  read_only
        .address_space:  global
        .offset:         72
        .size:           8
        .value_kind:     global_buffer
      - .actual_access:  write_only
        .address_space:  global
        .offset:         80
        .size:           8
        .value_kind:     global_buffer
    .group_segment_fixed_size: 4096
    .kernarg_segment_align: 8
    .kernarg_segment_size: 88
    .language:       OpenCL C
    .language_version:
      - 2
      - 0
    .max_flat_workgroup_size: 256
    .name:           _Z10scan_pass1PKDF16_S0_PKfS0_S2_S2_PDF16_PfS4_S2_S3_
    .private_segment_fixed_size: 0
    .sgpr_count:     94
    .sgpr_spill_count: 0
    .symbol:         _Z10scan_pass1PKDF16_S0_PKfS0_S2_S2_PDF16_PfS4_S2_S3_.kd
    .uniform_work_group_size: 1
    .uses_dynamic_stack: false
    .vgpr_count:     128
    .vgpr_spill_count: 0
    .wavefront_size: 64
  - .agpr_count:     0
    .args:
      - .actual_access:  read_only
        .address_space:  global
        .offset:         0
        .size:           8
        .value_kind:     global_buffer
      - .actual_access:  read_only
        .address_space:  global
        .offset:         8
        .size:           8
        .value_kind:     global_buffer
      - .actual_access:  read_only
        .address_space:  global
        .offset:         16
        .size:           8
        .value_kind:     global_buffer
      - .actual_access:  read_only
        .address_space:  global
        .offset:         24
        .size:           8
        .value_kind:     global_buffer
      - .actual_access:  read_only
        .address_space:  global
        .offset:         32
        .size:           8
        .value_kind:     global_buffer
      - .actual_access:  read_only
        .address_space:  global
        .offset:         40
        .size:           8
        .value_kind:     global_buffer
      - .actual_access:  write_only
        .address_space:  global
        .offset:         48
        .size:           8
        .value_kind:     global_buffer
      - .actual_access:  read_only
        .address_space:  global
        .offset:         56
        .size:           8
        .value_kind:     global_buffer
    .group_segment_fixed_size: 4096
    .kernarg_segment_align: 8
    .kernarg_segment_size: 64
    .language:       OpenCL C
    .language_version:
      - 2
      - 0
    .max_flat_workgroup_size: 256
    .name:           _Z10scan_pass2PKDF16_PKfS2_S0_S2_S0_PDF16_S2_
    .private_segment_fixed_size: 0
    .sgpr_count:     104
    .sgpr_spill_count: 0
    .symbol:         _Z10scan_pass2PKDF16_PKfS2_S0_S2_S0_PDF16_S2_.kd
    .uniform_work_group_size: 1
    .uses_dynamic_stack: false
    .vgpr_count:     118
    .vgpr_spill_count: 0
    .wavefront_size: 64
  - .agpr_count:     0
    .args:
      - .actual_access:  read_only
        .address_space:  global
        .offset:         0
        .size:           8
        .value_kind:     global_buffer
      - .actual_access:  read_only
        .address_space:  global
        .offset:         8
        .size:           8
        .value_kind:     global_buffer
      - .actual_access:  read_only
        .address_space:  global
        .offset:         16
        .size:           8
        .value_kind:     global_buffer
      - .actual_access:  write_only
        .address_space:  global
        .offset:         24
        .size:           8
        .value_kind:     global_buffer
    .group_segment_fixed_size: 8192
    .kernarg_segment_align: 8
    .kernarg_segment_size: 32
    .language:       OpenCL C
    .language_version:
      - 2
      - 0
    .max_flat_workgroup_size: 512
    .name:           _Z12scan_combinePKfPKDF16_S0_PDF16_
    .private_segment_fixed_size: 0
    .sgpr_count:     32
    .sgpr_spill_count: 0
    .symbol:         _Z12scan_combinePKfPKDF16_S0_PDF16_.kd
    .uniform_work_group_size: 1
    .uses_dynamic_stack: false
    .vgpr_count:     120
    .vgpr_spill_count: 0
    .wavefront_size: 64
  - .agpr_count:     0
    .args:
      - .address_space:  global
        .offset:         0
        .size:           8
        .value_kind:     global_buffer
      - .address_space:  global
        .offset:         8
        .size:           8
        .value_kind:     global_buffer
      - .actual_access:  write_only
        .address_space:  global
        .offset:         16
        .size:           8
        .value_kind:     global_buffer
      - .actual_access:  read_only
        .address_space:  global
        .offset:         24
        .size:           8
        .value_kind:     global_buffer
      - .offset:         32
        .size:           4
        .value_kind:     by_value
      - .actual_access:  read_only
        .address_space:  global
        .offset:         40
        .size:           8
        .value_kind:     global_buffer
    .group_segment_fixed_size: 0
    .kernarg_segment_align: 8
    .kernarg_segment_size: 48
    .language:       OpenCL C
    .language_version:
      - 2
      - 0
    .max_flat_workgroup_size: 512
    .name:           _Z11gemm_8phaseILi0ELi16ELi16ELi1024ELi1024ELi4096ELi1EEvPKDF16_S1_PvS2_fPj
    .private_segment_fixed_size: 0
    .sgpr_count:     40
    .sgpr_spill_count: 0
    .symbol:         _Z11gemm_8phaseILi0ELi16ELi16ELi1024ELi1024ELi4096ELi1EEvPKDF16_S1_PvS2_fPj.kd
    .uniform_work_group_size: 1
    .uses_dynamic_stack: false
    .vgpr_count:     236
    .vgpr_spill_count: 0
    .wavefront_size: 64
  - .agpr_count:     0
    .args:
      - .address_space:  global
        .offset:         0
        .size:           8
        .value_kind:     global_buffer
      - .address_space:  global
        .offset:         8
        .size:           8
        .value_kind:     global_buffer
      - .actual_access:  write_only
        .address_space:  global
        .offset:         16
        .size:           8
        .value_kind:     global_buffer
      - .address_space:  global
        .offset:         24
        .size:           8
        .value_kind:     global_buffer
      - .offset:         32
        .size:           4
        .value_kind:     by_value
      - .address_space:  global
        .offset:         40
        .size:           8
        .value_kind:     global_buffer
    .group_segment_fixed_size: 0
    .kernarg_segment_align: 8
    .kernarg_segment_size: 48
    .language:       OpenCL C
    .language_version:
      - 2
      - 0
    .max_flat_workgroup_size: 512
    .name:           _Z11gemm_8phaseILi1ELi16ELi4ELi512ELi2048ELi1024ELi4EEvPKDF16_S1_PvS2_fPj
    .private_segment_fixed_size: 0
    .sgpr_count:     41
    .sgpr_spill_count: 0
    .symbol:         _Z11gemm_8phaseILi1ELi16ELi4ELi512ELi2048ELi1024ELi4EEvPKDF16_S1_PvS2_fPj.kd
    .uniform_work_group_size: 1
    .uses_dynamic_stack: false
    .vgpr_count:     236
    .vgpr_spill_count: 0
    .wavefront_size: 64
  - .agpr_count:     0
    .args:
      - .address_space:  global
        .offset:         0
        .size:           8
        .value_kind:     global_buffer
      - .address_space:  global
        .offset:         8
        .size:           8
        .value_kind:     global_buffer
      - .actual_access:  write_only
        .address_space:  global
        .offset:         16
        .size:           8
        .value_kind:     global_buffer
      - .address_space:  global
        .offset:         24
        .size:           8
        .value_kind:     global_buffer
      - .offset:         32
        .size:           4
        .value_kind:     by_value
      - .address_space:  global
        .offset:         40
        .size:           8
        .value_kind:     global_buffer
    .group_segment_fixed_size: 0
    .kernarg_segment_align: 8
    .kernarg_segment_size: 48
    .language:       OpenCL C
    .language_version:
      - 2
      - 0
    .max_flat_workgroup_size: 512
    .name:           _Z11gemm_8phaseILi2ELi16ELi4ELi512ELi2048ELi1024ELi4EEvPKDF16_S1_PvS2_fPj
    .private_segment_fixed_size: 0
    .sgpr_count:     44
    .sgpr_spill_count: 0
    .symbol:         _Z11gemm_8phaseILi2ELi16ELi4ELi512ELi2048ELi1024ELi4EEvPKDF16_S1_PvS2_fPj.kd
    .uniform_work_group_size: 1
    .uses_dynamic_stack: false
    .vgpr_count:     236
    .vgpr_spill_count: 0
    .wavefront_size: 64
